# attention: per-thread K/V LDS-DMA source offsets precomputed once into 16 KiB extra static LDS; selected and window stage loops issue the 4 DMAs via saddr+offset with no per-stage vector address arith
# speedup vs baseline: 1.0151x; 1.0057x over previous
.LBB0_895:
	v_lshl_add_u64 v[6:7], v[2:3], 2, s[6:7]
	global_load_dword v5, v[6:7], off
	v_add_u32_e32 v4, 0x200, v4
	v_cmp_lt_u32_e32 vcc, s2, v4
	v_add_u32_e32 v2, 4, v2
	s_or_b64 s[0:1], vcc, s[0:1]
	s_waitcnt vmcnt(0)
	v_mul_f32_e32 v5, 0x3fb8aa3b, v5
	ds_write_b32 v1, v5
	v_add_u32_e32 v1, 0x800, v1
	s_andn2_b64 exec, exec, s[0:1]
	s_cbranch_execnz .LBB0_895
	s_or_b64 exec, exec, s[0:1]
	v_lshrrev_b32_e32 v5, 6, v0
	v_lshrrev_b32_e32 v6, 4, v166
	v_lshl_add_u32 v6, v5, 3, v6
	v_add_u32_e32 v7, 4, v6
	v_and_b32_e32 v8, 0xffffffe0, v6
	v_lshlrev_b32_e32 v1, 1, v6
	v_and_b32_e32 v1, 24, v1
	v_lshrrev_b32_e32 v2, 2, v6
	v_and_b32_e32 v2, 4, v2
	v_or3_b32 v8, v8, v1, v2
	v_and_b32_e32 v1, 3, v6
	v_or_b32_e32 v8, v8, v1
	v_xor_b32_e32 v9, v6, v166
	v_and_b32_e32 v9, 15, v9
	v_lshlrev_b32_e32 v9, 4, v9
	v_and_b32_e32 v10, 0xffffffe0, v7
	v_lshlrev_b32_e32 v1, 1, v7
	v_and_b32_e32 v1, 24, v1
	v_lshrrev_b32_e32 v2, 2, v7
	v_and_b32_e32 v2, 4, v2
	v_or3_b32 v10, v10, v1, v2
	v_and_b32_e32 v1, 3, v7
	v_or_b32_e32 v10, v10, v1
	v_xor_b32_e32 v11, v7, v166
	v_and_b32_e32 v11, 15, v11
	v_lshlrev_b32_e32 v11, 4, v11
	v_lshrrev_b32_e32 v16, 3, v166
	v_lshl_add_u32 v16, v5, 4, v16
	v_add_u32_e32 v17, 8, v16
	v_lshrrev_b32_e32 v18, 1, v16
	v_xor_b32_e32 v18, v18, v166
	v_and_b32_e32 v18, 7, v18
	v_lshlrev_b32_e32 v18, 4, v18
	v_lshrrev_b32_e32 v19, 1, v17
	v_xor_b32_e32 v19, v19, v166
	v_and_b32_e32 v19, 7, v19
	v_lshlrev_b32_e32 v19, 4, v19
	v_lshl_or_b32 v12, v8, 8, v9
	v_lshl_or_b32 v13, v10, 8, v11
	v_lshl_or_b32 v14, v16, 10, v18
	v_lshl_or_b32 v15, v17, 10, v19
	v_lshl_or_b32 v20, v8, 12, v9
	v_lshl_or_b32 v21, v10, 12, v11
	v_lshl_or_b32 v22, v16, 15, v18
	v_lshl_or_b32 v23, v17, 15, v19
	v_lshlrev_b32_e32 v1, 4, v0
	v_add_u32_e32 v1, 0x24000, v1
	ds_write_b128 v1, v[12:15]
	ds_write_b128 v1, v[20:23] offset:8192
	s_cmpk_gt_i32 s90, 0x3ff
	s_waitcnt lgkmcnt(0)
	s_barrier
	s_cbranch_scc1 .LBB0_1273
	v_writelane_b32 v255, s40, 11
	v_cmp_ne_u32_e64 s[10:11], 0, v166
	v_and_b32_e32 v1, 15, v0
	v_writelane_b32 v255, s41, 12
	v_writelane_b32 v255, s62, 13
	v_bfe_u32 v230, v0, 2, 2
	v_lshrrev_b32_e32 v4, 4, v166
	v_writelane_b32 v255, s63, 14
	v_writelane_b32 v255, s10, 15
	v_bitop3_b32 v5, v4, v0, 15 bitop3:0x78
	v_lshlrev_b32_e32 v209, 4, v5
	v_writelane_b32 v255, s11, 16
	v_cmp_eq_u32_e64 s[10:11], 0, v166
	v_bitop3_b32 v5, v4, v1, 4 bitop3:0x36
	v_lshlrev_b32_e32 v210, 4, v5
	v_writelane_b32 v255, s10, 17
	v_bitop3_b32 v5, v4, v1, 8 bitop3:0x36
	s_lshl_b32 s0, s92, 12
	v_writelane_b32 v255, s11, 18
	v_cmp_gt_u32_e64 s[10:11], 4, v1
	v_and_b32_e32 v2, 48, v166
	v_mov_b32_e32 v3, 0
	v_writelane_b32 v255, s10, 19
	s_lshl_b32 s8, s92, 11
	v_lshlrev_b32_e32 v211, 4, v5
	v_writelane_b32 v255, s11, 20
	v_cmp_eq_u32_e64 s[10:11], 1, v230
	v_bitop3_b32 v5, v4, v1, 12 bitop3:0x36
	v_lshl_add_u64 v[252:253], s[62:63], 0, v[2:3]
	v_writelane_b32 v255, s10, 21
	s_add_i32 s1, s0, 0
	s_sub_i32 s6, 0, s8
	v_writelane_b32 v255, s11, 22
	v_cmp_eq_u32_e64 s[10:11], 2, v230
	v_lshlrev_b32_e32 v2, 8, v1
	v_lshlrev_b32_e32 v212, 4, v5
	v_writelane_b32 v255, s10, 23
	s_mov_b32 s7, 0xa000
	v_add_u32_e32 v218, 0, v2
	v_writelane_b32 v255, s11, 24
	v_cmp_eq_u32_e64 s[10:11], 3, v230
	v_or3_b32 v232, v2, v212, s7
	v_or3_b32 v233, v2, v211, s7
	v_writelane_b32 v255, s10, 25
	v_or3_b32 v234, v2, v210, s7
	v_or3_b32 v235, v2, v209, s7
	v_writelane_b32 v255, s11, 26
	v_writelane_b32 v255, s8, 27
	v_lshl_or_b32 v2, v230, 9, s0
	s_add_i32 s0, s1, s6
	v_writelane_b32 v255, s0, 28
	s_add_i32 s0, 0, 0x12000
	v_writelane_b32 v255, s0, 29
	s_add_i32 s0, 0, 0x16000
	v_writelane_b32 v255, s0, 30
	v_add_u32_e32 v5, 48, v0
	v_bfe_u32 v6, v0, 1, 3
	v_writelane_b32 v255, s96, 31
	s_lshl_b32 s73, s92, 3
	s_lshl_b32 s81, s92, 4
	v_and_b32_e32 v213, 63, v5
	v_lshlrev_b32_e32 v5, 7, v1
	v_xor_b32_e32 v7, v6, v4
	v_bitop3_b32 v6, v4, v6, 4 bitop3:0x36
	v_mul_i32_i24_e32 v1, -8, v4
	v_writelane_b32 v255, s97, 32
	v_and_b32_e32 v179, 3, v0
	v_lshlrev_b32_e32 v208, 3, v4
	s_or_b32 s65, s73, 4
	s_or_b32 s78, s81, 8
	v_lshlrev_b32_e32 v216, 2, v4
	v_lshl_add_u32 v215, v166, 2, s1
	v_lshlrev_b32_e32 v4, 7, v4
	v_lshl_or_b32 v220, v6, 4, v5
	v_lshl_or_b32 v225, v7, 4, v5
	v_or_b32_e32 v239, v1, v230
	v_mbcnt_lo_u32_b32 v1, -1, 0
	v_writelane_b32 v254, s60, 7
	v_writelane_b32 v255, s94, 33
	s_lshl_b32 s85, s65, 8
	s_lshl_b32 s40, s78, 7
	v_cmp_gt_u32_e64 s[2:3], 16, v166
	v_cmp_eq_u32_e64 s[4:5], 0, v179
	v_or_b32_e32 v214, 64, v166
	v_add_u32_e32 v217, 0x2000, v215
	v_or_b32_e32 v247, 0xffffffc0, v166
	v_sub_u32_e32 v219, v230, v4
	s_add_i32 s33, s8, 0
	v_or_b32_e32 v221, 0x10000, v220
	v_or_b32_e32 v222, 0x10800, v220
	v_or_b32_e32 v223, 0x11000, v220
	v_or_b32_e32 v224, 0x11800, v220
	v_or_b32_e32 v226, 0x10000, v225
	v_or_b32_e32 v227, 0x10800, v225
	v_or_b32_e32 v228, 0x11000, v225
	v_or_b32_e32 v229, 0x11800, v225
	v_or_b32_e32 v231, 0x270, v4
	s_add_i32 s64, s8, 0x1e400
	s_add_i32 s80, s8, 0x1a400
	s_add_i32 s79, s8, 0x1e000
	s_add_i32 s58, s8, 0x1a000
	v_add_u32_e32 v236, 0, v208
	v_add_u32_e32 v237, 0x2000, v2
	v_sub_u32_e32 v238, v230, v208
	s_movk_i32 s59, 0xff84
	v_mov_b32_e32 v173, 0x41000000
	s_movk_i32 s62, 0x200
	v_lshlrev_b32_e32 v174, 2, v216
	v_mov_b32_e32 v176, 0xf149f2ca
	v_mov_b32_e32 v240, 0x9e
	v_mov_b32_e32 v241, 0xff61b1e6
	v_mbcnt_hi_u32_b32 v242, -1, v1
	v_mov_b32_e32 v243, 0x7f
	s_mov_b32 s63, s90
	v_writelane_b32 v254, s61, 8
	v_writelane_b32 v255, s95, 34
	s_branch .LBB0_899

.LBB0_1132:
	s_mov_b32 s6, 0x26000
	s_cmp_eq_u32 s42, 0x80
	s_cselect_b32 s6, 0x24000, s6
	v_lshl_add_u32 v118, v0, 4, s6
	ds_read_b128 v[118:121], v118
	s_mul_hi_u32 s1, s47, 0xaaaaaaab
	s_lshr_b32 s1, s1, 1
	s_mul_i32 s1, s1, 0x18000
	s_sub_i32 s21, s64, s1
	s_sub_i32 s38, s80, s1
	s_sub_i32 s39, s79, s1
	s_sub_i32 s1, s58, s1
	s_mul_i32 s6, s0, s42
	s_lshl_b32 s6, s6, 1
	s_add_u32 s98, s34, s6
	s_addc_u32 s99, s35, 0
	s_lshl_b32 s6, s0, 1
	s_add_u32 s100, s18, s6
	s_addc_u32 s101, s19, 0
	s_add_i32 s1, s8, s1
	s_add_i32 m0, s9, s1
	s_waitcnt lgkmcnt(0)
	global_load_lds_dwordx4 v118, s[98:99]
	s_add_i32 s1, s8, s38
	s_add_i32 m0, s9, s1
	s_nop 0
	global_load_lds_dwordx4 v119, s[98:99]
	s_add_i32 s6, s8, s39
	s_add_i32 m0, s9, s6
	s_nop 0
	global_load_lds_dwordx4 v120, s[100:101]
	s_add_i32 s0, s8, s21
	s_add_i32 m0, s9, s0
	s_nop 0
	global_load_lds_dwordx4 v121, s[100:101]

.LBB0_1202:
	s_mov_b32 s6, 0x26000
	s_cmp_eq_u32 s42, 0x80
	s_cselect_b32 s6, 0x24000, s6
	v_lshl_add_u32 v118, v0, 4, s6
	ds_read_b128 v[118:121], v118
	s_mul_hi_u32 s6, s45, 0xaaaaaaab
	s_lshr_b32 s6, s6, 1
	s_mul_i32 s6, s6, 0x18000
	s_sub_i32 s35, s64, s6
	s_sub_i32 s19, s80, s6
	s_sub_i32 s38, s79, s6
	s_sub_i32 s39, s58, s6
	s_mul_i32 s6, s18, s42
	s_lshl_b32 s6, s6, 1
	s_add_u32 s98, s36, s6
	s_addc_u32 s99, s37, 0
	s_lshl_b32 s6, s18, 1
	s_add_u32 s100, s20, s6
	s_addc_u32 s101, s21, 0
	s_add_i32 s6, s47, s39
	s_add_i32 m0, s15, s6
	s_waitcnt lgkmcnt(0)
	global_load_lds_dwordx4 v118, s[98:99]
	s_add_i32 s6, s47, s19
	s_add_i32 m0, s15, s6
	s_nop 0
	global_load_lds_dwordx4 v119, s[98:99]
	s_add_i32 s18, s47, s38
	s_add_i32 m0, s15, s18
	s_nop 0
	global_load_lds_dwordx4 v120, s[100:101]
	s_add_i32 s6, s47, s35
	s_add_i32 m0, s15, s6
	s_nop 0
	global_load_lds_dwordx4 v121, s[100:101]

	.amdhsa_kernel _Z10fwd_kernel4Args
		.amdhsa_group_segment_fixed_size 16384
		.amdhsa_private_segment_fixed_size 0
		.amdhsa_kernarg_size 464
		.amdhsa_user_sgpr_count 2
		.amdhsa_user_sgpr_dispatch_ptr 0
		.amdhsa_user_sgpr_queue_ptr 0
		.amdhsa_user_sgpr_kernarg_segment_ptr 1
		.amdhsa_user_sgpr_dispatch_id 0
		.amdhsa_user_sgpr_kernarg_preload_length 0
		.amdhsa_user_sgpr_kernarg_preload_offset 0
		.amdhsa_user_sgpr_private_segment_size 0
		.amdhsa_uses_dynamic_stack 0
		.amdhsa_enable_private_segment 0
		.amdhsa_system_sgpr_workgroup_id_x 1
		.amdhsa_system_sgpr_workgroup_id_y 0
		.amdhsa_system_sgpr_workgroup_id_z 0
		.amdhsa_system_sgpr_workgroup_info 0
		.amdhsa_system_vgpr_workitem_id 0
		.amdhsa_next_free_vgpr 256
		.amdhsa_next_free_sgpr 102
		.amdhsa_accum_offset 256
		.amdhsa_reserve_vcc 1
		.amdhsa_float_round_mode_32 0
		.amdhsa_float_round_mode_16_64 0
		.amdhsa_float_denorm_mode_32 3
		.amdhsa_float_denorm_mode_16_64 3
		.amdhsa_dx10_clamp 1
		.amdhsa_ieee_mode 1
		.amdhsa_fp16_overflow 0
		.amdhsa_tg_split 0
		.amdhsa_exception_fp_ieee_invalid_op 0
		.amdhsa_exception_fp_denorm_src 0
		.amdhsa_exception_fp_ieee_div_zero 0
		.amdhsa_exception_fp_ieee_overflow 0
		.amdhsa_exception_fp_ieee_underflow 0
		.amdhsa_exception_fp_ieee_inexact 0
		.amdhsa_exception_int_div_zero 0
	.end_amdhsa_kernel

.Lfunc_end0:
	.size	_Z10fwd_kernel4Args, .Lfunc_end0-_Z10fwd_kernel4Args
	.set _Z10fwd_kernel4Args.num_vgpr, 256
	.set _Z10fwd_kernel4Args.num_agpr, 0
	.set _Z10fwd_kernel4Args.numbered_sgpr, 102
	.set _Z10fwd_kernel4Args.num_named_barrier, 0
	.set _Z10fwd_kernel4Args.private_seg_size, 0
	.set _Z10fwd_kernel4Args.uses_vcc, 1
	.set _Z10fwd_kernel4Args.uses_flat_scratch, 0
	.set _Z10fwd_kernel4Args.has_dyn_sized_stack, 0
	.set _Z10fwd_kernel4Args.has_recursion, 0
	.set _Z10fwd_kernel4Args.has_indirect_call, 0

amdhsa.kernels:
  - .agpr_count:     0
    .args:
      - .offset:         0
        .size:           208
        .value_kind:     by_value
      - .offset:         208
        .size:           4
        .value_kind:     hidden_block_count_x
      - .offset:         212
        .size:           4
        .value_kind:     hidden_block_count_y
      - .offset:         216
        .size:           4
        .value_kind:     hidden_block_count_z
      - .offset:         220
        .size:           2
        .value_kind:     hidden_group_size_x
      - .offset:         222
        .size:           2
        .value_kind:     hidden_group_size_y
      - .offset:         224
        .size:           2
        .value_kind:     hidden_group_size_z
      - .offset:         226
        .size:           2
        .value_kind:     hidden_remainder_x
      - .offset:         228
        .size:           2
        .value_kind:     hidden_remainder_y
      - .offset:         230
        .size:           2
        .value_kind:     hidden_remainder_z
      - .offset:         248
        .size:           8
        .value_kind:     hidden_global_offset_x
      - .offset:         256
        .size:           8
        .value_kind:     hidden_global_offset_y
      - .offset:         264
        .size:           8
        .value_kind:     hidden_global_offset_z
      - .offset:         272
        .size:           2
        .value_kind:     hidden_grid_dims
      - .offset:         328
        .size:           4
        .value_kind:     hidden_dynamic_lds_size
    .group_segment_fixed_size: 16384
    .kernarg_segment_align: 8
    .kernarg_segment_size: 464
    .language:       OpenCL C
    .language_version:
      - 2
      - 0
    .max_flat_workgroup_size: 512
    .name:           _Z10fwd_kernel4Args
    .private_segment_fixed_size: 0
    .sgpr_count:     108
    .sgpr_spill_count: 103
    .symbol:         _Z10fwd_kernel4Args.kd
    .uniform_work_group_size: 1
    .uses_dynamic_stack: false
    .vgpr_count:     256
    .vgpr_spill_count: 0
    .wavefront_size: 64
